# v50 with nt (streaming) hint on the in-projection and down-projection epilogue stores
# speedup vs baseline: 1.0165x; 1.0165x over previous
; __device__ __forceinline__ unsigned cvt_pk_bf16(float lo, float hi) { unsigned r; asm volatile("v_cvt_pk_bf16_f32 %0, %1, %2" : "=v"(r) : "v"(lo), "v"(hi)); return r; }
;     __device__ __forceinline__ void operator()(const f32x4 (&acc)[2][2][4][2], const pg8::Unit& u, int wr, int wc, int fr, int fq) const {
;     ...
;                 float rstd = 1.f;
;                 if (nrm) {
;                     float ss = 0.f;
; #pragma unroll
;                     for (int bj = 0; bj < 2; ++bj)
; #pragma unroll
;                         for (int n = 0; n < 2; ++n) ss += (v[bj][n][0] * v[bj][n][0] + v[bj][n][1] * v[bj][n][1]) + (v[bj][n][2] * v[bj][n][2] + v[bj][n][3] * v[bj][n][3]);
;                     ss += __shfl_xor(ss, 16); ss += __shfl_xor(ss, 32);
;                     rstd = rsqrtf(ss * (1.f / 64.f) + RMS_EPS);
;                 }
;                 if (st == ST_G) {
; #pragma unroll
;                     for (int bj = 0; bj < 2; ++bj)
; #pragma unroll
;                         for (int n = 0; n < 2; ++n)
; #pragma unroll
;                             for (int j = 0; j < 4; ++j) v[bj][n][j] = __builtin_amdgcn_rcpf(1.f + __expf(-v[bj][n][j]));
;                 }
;                 bf16_t* rowp = base + (size_t)(ai * 128 + m * 16) * 64;
; #pragma unroll
;                 for (int bj = 0; bj < 2; ++bj) {
;                     const f32x4 v0 = v[bj][0] * rstd * g[bj][0], v1 = v[bj][1] * rstd * g[bj][1];
;                     u32x4 w; w.x = pg8::cvt_pk_bf16(v0[0], v0[1]); w.y = pg8::cvt_pk_bf16(v0[2], v0[3]); w.z = pg8::cvt_pk_bf16(v1[0], v1[1]); w.w = pg8::cvt_pk_bf16(v1[2], v1[3]);
;                     *(u32x4*)(rowp + 32 * bj) = w;
;                 }
.LBB0_240:
	s_ashr_i32 s23, s22, 31
	s_ashr_i32 s9, s8, 31
	s_lshl_b64 s[22:23], s[22:23], 22
	s_lshl_b64 s[8:9], s[8:9], 15
	s_add_u32 s15, s96, s22
	s_addc_u32 s17, s97, s23
	s_add_u32 s8, s15, s8
	s_addc_u32 s9, s17, s9
	v_lshl_add_u64 v[162:163], s[8:9], 0, v[150:151]
	v_pk_mul_f32 v[140:141], v[164:165], v[140:141] op_sel_hi:[0,1]
	v_pk_mul_f32 v[138:139], v[164:165], v[138:139] op_sel_hi:[0,1]
	v_pk_mul_f32 v[136:137], v[164:165], v[136:137] op_sel_hi:[0,1]
	v_pk_mul_f32 v[134:135], v[164:165], v[134:135] op_sel_hi:[0,1]
	v_lshl_add_u64 v[162:163], v[162:163], 0, v[34:35]
	v_pk_mul_f32 v[140:141], v[156:157], v[140:141]
	v_pk_mul_f32 v[138:139], v[62:63], v[138:139]
	v_pk_mul_f32 v[168:169], v[158:159], v[136:137]
	v_pk_mul_f32 v[136:137], v[64:65], v[134:135]
	v_cvt_pk_bf16_f32 v134, v138, v139
	v_cvt_pk_bf16_f32 v135, v140, v141
	v_pk_mul_f32 v[130:131], v[164:165], v[130:131] op_sel_hi:[0,1]
	v_pk_mul_f32 v[128:129], v[164:165], v[128:129] op_sel_hi:[0,1]
	v_pk_mul_f32 v[126:127], v[164:165], v[126:127] op_sel_hi:[0,1]
	v_cvt_pk_bf16_f32 v136, v136, v137
	v_cvt_pk_bf16_f32 v137, v168, v169
	global_store_dwordx4 v[162:163], v[134:137], off nt
	v_pk_mul_f32 v[132:133], v[164:165], v[132:133] op_sel_hi:[0,1]
	v_pk_mul_f32 v[130:131], v[66:67], v[130:131]
	v_pk_mul_f32 v[134:135], v[160:161], v[128:129]
	v_pk_mul_f32 v[128:129], v[52:53], v[126:127]
	v_cvt_pk_bf16_f32 v126, v130, v131
	v_pk_mul_f32 v[132:133], v[68:69], v[132:133]
	s_and_b64 vcc, exec, s[6:7]
	v_cvt_pk_bf16_f32 v127, v132, v133
	v_cvt_pk_bf16_f32 v128, v128, v129
	v_cvt_pk_bf16_f32 v129, v134, v135
	global_store_dwordx4 v[162:163], v[126:129], off offset:64 nt
	s_nop 1
	v_mov_b32_e32 v126, 1.0
	s_cbranch_vccnz .LBB0_242
	v_pk_mul_f32 v[126:127], v[124:125], v[124:125]
	v_pk_mul_f32 v[128:129], v[122:123], v[122:123]
	v_cmp_lt_i32_e32 vcc, v236, v241
	v_pk_mov_b32 v[130:131], v[128:129], v[126:127] op_sel:[1,0]
	v_mov_b32_e32 v129, v127
	v_pk_add_f32 v[126:127], v[130:131], v[128:129]
	v_pk_mul_f32 v[128:129], v[120:121], v[120:121]
	v_pk_mul_f32 v[130:131], v[118:119], v[118:119]
	v_pk_add_f32 v[126:127], v[126:127], v[126:127] op_sel:[0,1] op_sel_hi:[1,0]
	v_pk_mov_b32 v[132:133], v[130:131], v[128:129] op_sel:[1,0]
	v_mov_b32_e32 v131, v129
	v_pk_add_f32 v[128:129], v[132:133], v[130:131]
	v_mul_f32_e32 v130, v110, v110
	v_mul_f32_e32 v131, v111, v111
	v_pk_add_f32 v[128:129], v[128:129], v[128:129] op_sel:[0,1] op_sel_hi:[1,0]
	v_mov_b32_e32 v127, v130
	v_mov_b32_e32 v129, v131
	v_pk_add_f32 v[126:127], v[126:127], v[128:129]
	v_mul_f32_e32 v128, v115, v115
	v_mul_f32_e32 v130, v117, v117
	v_mul_f32_e32 v132, v112, v112
	v_mul_f32_e32 v133, v113, v113
	v_pk_fma_f32 v[128:129], v[114:115], v[114:115], v[128:129] op_sel_hi:[1,1,0]
	v_pk_fma_f32 v[130:131], v[116:117], v[116:117], v[130:131] op_sel_hi:[1,1,0]
	v_mov_b32_e32 v129, v132
	v_mov_b32_e32 v131, v133
	v_pk_add_f32 v[128:129], v[128:129], v[130:131]
	s_nop 0
	v_pk_add_f32 v[126:127], v[126:127], v[128:129]
	s_nop 0
	v_add_f32_e32 v126, v126, v127
	v_cndmask_b32_e32 v127, v199, v236, vcc
	v_lshlrev_b32_e32 v127, 2, v127
	ds_bpermute_b32 v127, v127, v126
	v_cmp_lt_i32_e32 vcc, v237, v241
	s_waitcnt lgkmcnt(0)
	v_add_f32_e32 v126, v126, v127
	v_cndmask_b32_e32 v127, v199, v237, vcc
	v_lshlrev_b32_e32 v127, 2, v127
	ds_bpermute_b32 v127, v127, v126
	s_waitcnt lgkmcnt(0)
	v_add_f32_e32 v126, v126, v127
	v_fmamk_f32 v126, v126, 0x3c800000, v198
	v_mul_f32_e32 v127, 0x4b800000, v126
	v_cmp_gt_f32_e32 vcc, s76, v126
	s_nop 1
	v_cndmask_b32_e32 v126, v126, v127, vcc
	v_rsq_f32_e32 v126, v126
	s_nop 0
	v_mul_f32_e32 v127, 0x45800000, v126
	v_cndmask_b32_e32 v126, v126, v127, vcc

; __device__ __forceinline__ unsigned cvt_pk_bf16(float lo, float hi) { unsigned r; asm volatile("v_cvt_pk_bf16_f32 %0, %1, %2" : "=v"(r) : "v"(lo), "v"(hi)); return r; }
;     __device__ __forceinline__ void operator()(const f32x4 (&acc)[2][2][4][2], const pg8::Unit& u, int wr, int wc, int fr, int fq) const {
;     ...
;                 bf16_t* rowp = base + (size_t)(ai * 128 + m * 16) * 64;
; #pragma unroll
;                 for (int bj = 0; bj < 2; ++bj) {
;                     const f32x4 v0 = v[bj][0] * rstd * g[bj][0], v1 = v[bj][1] * rstd * g[bj][1];
;                     u32x4 w; w.x = pg8::cvt_pk_bf16(v0[0], v0[1]); w.y = pg8::cvt_pk_bf16(v0[2], v0[3]); w.z = pg8::cvt_pk_bf16(v1[0], v1[1]); w.w = pg8::cvt_pk_bf16(v1[2], v1[3]);
;                     *(u32x4*)(rowp + 32 * bj) = w;
;                 }
.LBB0_246:
	v_pk_mul_f32 v[124:125], v[126:127], v[124:125] op_sel_hi:[0,1]
	v_pk_mul_f32 v[122:123], v[126:127], v[122:123] op_sel_hi:[0,1]
	v_pk_mul_f32 v[120:121], v[126:127], v[120:121] op_sel_hi:[0,1]
	v_pk_mul_f32 v[118:119], v[126:127], v[118:119] op_sel_hi:[0,1]
	v_pk_mul_f32 v[124:125], v[156:157], v[124:125]
	v_pk_mul_f32 v[122:123], v[62:63], v[122:123]
	v_pk_mul_f32 v[128:129], v[158:159], v[120:121]
	v_pk_mul_f32 v[120:121], v[64:65], v[118:119]
	v_cvt_pk_bf16_f32 v118, v122, v123
	v_cvt_pk_bf16_f32 v119, v124, v125
	v_pk_mul_f32 v[114:115], v[126:127], v[114:115] op_sel_hi:[0,1]
	v_pk_mul_f32 v[112:113], v[126:127], v[112:113] op_sel_hi:[0,1]
	v_pk_mul_f32 v[110:111], v[126:127], v[110:111] op_sel_hi:[0,1]
	v_cvt_pk_bf16_f32 v120, v120, v121
	v_cvt_pk_bf16_f32 v121, v128, v129
	global_store_dwordx4 v[162:163], v[118:121], off offset:2048 nt
	v_pk_mul_f32 v[116:117], v[126:127], v[116:117] op_sel_hi:[0,1]
	v_pk_mul_f32 v[114:115], v[66:67], v[114:115]
	v_pk_mul_f32 v[118:119], v[160:161], v[112:113]
	v_pk_mul_f32 v[112:113], v[52:53], v[110:111]
	v_cvt_pk_bf16_f32 v110, v114, v115
	v_pk_mul_f32 v[116:117], v[68:69], v[116:117]
	s_and_b64 vcc, exec, s[6:7]
	v_cvt_pk_bf16_f32 v111, v116, v117
	v_cvt_pk_bf16_f32 v112, v112, v113
	v_cvt_pk_bf16_f32 v113, v118, v119
	global_store_dwordx4 v[162:163], v[110:113], off offset:2112 nt
	s_nop 1
	v_mov_b32_e32 v110, 1.0
	s_cbranch_vccz .LBB0_251
	s_and_b64 vcc, exec, s[8:9]
	s_mov_b64 s[22:23], -1
	s_cbranch_vccnz .LBB0_252

; __device__ __forceinline__ unsigned cvt_pk_bf16(float lo, float hi) { unsigned r; asm volatile("v_cvt_pk_bf16_f32 %0, %1, %2" : "=v"(r) : "v"(lo), "v"(hi)); return r; }
;     __device__ __forceinline__ void operator()(const f32x4 (&acc)[2][2][4][2], const pg8::Unit& u, int wr, int wc, int fr, int fq) const {
;     ...
;                 float rstd = 1.f;
;                 if (nrm) {
;                     float ss = 0.f;
; #pragma unroll
;                     for (int bj = 0; bj < 2; ++bj)
; #pragma unroll
;                         for (int n = 0; n < 2; ++n) ss += (v[bj][n][0] * v[bj][n][0] + v[bj][n][1] * v[bj][n][1]) + (v[bj][n][2] * v[bj][n][2] + v[bj][n][3] * v[bj][n][3]);
;                     ss += __shfl_xor(ss, 16); ss += __shfl_xor(ss, 32);
;                     rstd = rsqrtf(ss * (1.f / 64.f) + RMS_EPS);
;                 }
;                 if (st == ST_G) {
; #pragma unroll
;                     for (int bj = 0; bj < 2; ++bj)
; #pragma unroll
;                         for (int n = 0; n < 2; ++n)
; #pragma unroll
;                             for (int j = 0; j < 4; ++j) v[bj][n][j] = __builtin_amdgcn_rcpf(1.f + __expf(-v[bj][n][j]));
;                 }
;                 bf16_t* rowp = base + (size_t)(ai * 128 + m * 16) * 64;
; #pragma unroll
;                 for (int bj = 0; bj < 2; ++bj) {
;                     const f32x4 v0 = v[bj][0] * rstd * g[bj][0], v1 = v[bj][1] * rstd * g[bj][1];
;                     u32x4 w; w.x = pg8::cvt_pk_bf16(v0[0], v0[1]); w.y = pg8::cvt_pk_bf16(v0[2], v0[3]); w.z = pg8::cvt_pk_bf16(v1[0], v1[1]); w.w = pg8::cvt_pk_bf16(v1[2], v1[3]);
;                     *(u32x4*)(rowp + 32 * bj) = w;
;                 }
.LBB0_254:
	v_pk_mul_f32 v[106:107], v[110:111], v[106:107] op_sel_hi:[0,1]
	v_pk_mul_f32 v[102:103], v[110:111], v[102:103] op_sel_hi:[0,1]
	v_pk_mul_f32 v[108:109], v[110:111], v[108:109] op_sel_hi:[0,1]
	v_pk_mul_f32 v[106:107], v[62:63], v[106:107]
	v_pk_mul_f32 v[104:105], v[110:111], v[104:105] op_sel_hi:[0,1]
	v_pk_mul_f32 v[102:103], v[64:65], v[102:103]
	v_pk_mul_f32 v[108:109], v[156:157], v[108:109]
	v_pk_mul_f32 v[112:113], v[158:159], v[104:105]
	v_cvt_pk_bf16_f32 v104, v106, v107
	v_cvt_pk_bf16_f32 v105, v108, v109
	v_cvt_pk_bf16_f32 v106, v102, v103
	v_add_co_u32_e32 v102, vcc, s33, v162
	v_pk_mul_f32 v[98:99], v[110:111], v[98:99] op_sel_hi:[0,1]
	s_nop 0
	v_addc_co_u32_e32 v103, vcc, 0, v163, vcc
	v_pk_mul_f32 v[96:97], v[110:111], v[96:97] op_sel_hi:[0,1]
	v_pk_mul_f32 v[94:95], v[110:111], v[94:95] op_sel_hi:[0,1]
	v_cvt_pk_bf16_f32 v107, v112, v113
	global_store_dwordx4 v[102:103], v[104:107], off nt
	v_pk_mul_f32 v[100:101], v[110:111], v[100:101] op_sel_hi:[0,1]
	v_pk_mul_f32 v[98:99], v[66:67], v[98:99]
	v_pk_mul_f32 v[104:105], v[160:161], v[96:97]
	v_pk_mul_f32 v[96:97], v[52:53], v[94:95]
	v_cvt_pk_bf16_f32 v94, v98, v99
	v_pk_mul_f32 v[100:101], v[68:69], v[100:101]
	s_and_b64 vcc, exec, s[6:7]
	v_cvt_pk_bf16_f32 v95, v100, v101
	v_cvt_pk_bf16_f32 v96, v96, v97
	v_cvt_pk_bf16_f32 v97, v104, v105
	global_store_dwordx4 v[102:103], v[94:97], off offset:64 nt
	s_nop 1
	v_mov_b32_e32 v94, 1.0
	s_cbranch_vccz .LBB0_257
	s_and_b64 vcc, exec, s[8:9]
	s_mov_b64 s[22:23], -1
	s_cbranch_vccnz .LBB0_258

; __device__ __forceinline__ unsigned cvt_pk_bf16(float lo, float hi) { unsigned r; asm volatile("v_cvt_pk_bf16_f32 %0, %1, %2" : "=v"(r) : "v"(lo), "v"(hi)); return r; }
;     __device__ __forceinline__ void operator()(const f32x4 (&acc)[2][2][4][2], const pg8::Unit& u, int wr, int wc, int fr, int fq) const {
;     ...
;                 bf16_t* rowp = base + (size_t)(ai * 128 + m * 16) * 64;
; #pragma unroll
;                 for (int bj = 0; bj < 2; ++bj) {
;                     const f32x4 v0 = v[bj][0] * rstd * g[bj][0], v1 = v[bj][1] * rstd * g[bj][1];
;                     u32x4 w; w.x = pg8::cvt_pk_bf16(v0[0], v0[1]); w.y = pg8::cvt_pk_bf16(v0[2], v0[3]); w.z = pg8::cvt_pk_bf16(v1[0], v1[1]); w.w = pg8::cvt_pk_bf16(v1[2], v1[3]);
;                     *(u32x4*)(rowp + 32 * bj) = w;
;                 }
.LBB0_260:
	v_pk_mul_f32 v[92:93], v[94:95], v[92:93] op_sel_hi:[0,1]
	v_pk_mul_f32 v[90:91], v[94:95], v[90:91] op_sel_hi:[0,1]
	v_pk_mul_f32 v[88:89], v[94:95], v[88:89] op_sel_hi:[0,1]
	v_pk_mul_f32 v[86:87], v[94:95], v[86:87] op_sel_hi:[0,1]
	v_pk_mul_f32 v[92:93], v[156:157], v[92:93]
	v_pk_mul_f32 v[90:91], v[62:63], v[90:91]
	v_pk_mul_f32 v[96:97], v[158:159], v[88:89]
	v_pk_mul_f32 v[88:89], v[64:65], v[86:87]
	v_cvt_pk_bf16_f32 v86, v90, v91
	v_cvt_pk_bf16_f32 v87, v92, v93
	v_pk_mul_f32 v[82:83], v[94:95], v[82:83] op_sel_hi:[0,1]
	v_pk_mul_f32 v[80:81], v[94:95], v[80:81] op_sel_hi:[0,1]
	v_pk_mul_f32 v[78:79], v[94:95], v[78:79] op_sel_hi:[0,1]
	v_cvt_pk_bf16_f32 v88, v88, v89
	v_cvt_pk_bf16_f32 v89, v96, v97
	global_store_dwordx4 v[102:103], v[86:89], off offset:2048 nt
	v_pk_mul_f32 v[84:85], v[94:95], v[84:85] op_sel_hi:[0,1]
	v_pk_mul_f32 v[82:83], v[66:67], v[82:83]
	v_pk_mul_f32 v[86:87], v[160:161], v[80:81]
	v_pk_mul_f32 v[80:81], v[52:53], v[78:79]
	v_cvt_pk_bf16_f32 v78, v82, v83
	v_pk_mul_f32 v[84:85], v[68:69], v[84:85]
	s_and_b64 vcc, exec, s[6:7]
	v_cvt_pk_bf16_f32 v79, v84, v85
	v_cvt_pk_bf16_f32 v80, v80, v81
	v_cvt_pk_bf16_f32 v81, v86, v87
	global_store_dwordx4 v[102:103], v[78:81], off offset:2112 nt
	s_nop 1
	v_mov_b32_e32 v78, 1.0
	s_cbranch_vccz .LBB0_263
	s_and_b64 vcc, exec, s[8:9]
	s_mov_b64 s[22:23], -1
	s_cbranch_vccnz .LBB0_264

; __device__ __forceinline__ unsigned cvt_pk_bf16(float lo, float hi) { unsigned r; asm volatile("v_cvt_pk_bf16_f32 %0, %1, %2" : "=v"(r) : "v"(lo), "v"(hi)); return r; }
;     __device__ __forceinline__ void operator()(const f32x4 (&acc)[2][2][4][2], const pg8::Unit& u, int wr, int wc, int fr, int fq) const {
;     ...
;                 bf16_t* rowp = base + (size_t)(ai * 128 + m * 16) * 64;
; #pragma unroll
;                 for (int bj = 0; bj < 2; ++bj) {
;                     const f32x4 v0 = v[bj][0] * rstd * g[bj][0], v1 = v[bj][1] * rstd * g[bj][1];
;                     u32x4 w; w.x = pg8::cvt_pk_bf16(v0[0], v0[1]); w.y = pg8::cvt_pk_bf16(v0[2], v0[3]); w.z = pg8::cvt_pk_bf16(v1[0], v1[1]); w.w = pg8::cvt_pk_bf16(v1[2], v1[3]);
;                     *(u32x4*)(rowp + 32 * bj) = w;
;                 }
.LBB0_266:
	v_pk_mul_f32 v[74:75], v[78:79], v[74:75] op_sel_hi:[0,1]
	v_pk_mul_f32 v[70:71], v[78:79], v[70:71] op_sel_hi:[0,1]
	v_pk_mul_f32 v[76:77], v[78:79], v[76:77] op_sel_hi:[0,1]
	v_pk_mul_f32 v[74:75], v[62:63], v[74:75]
	v_pk_mul_f32 v[72:73], v[78:79], v[72:73] op_sel_hi:[0,1]
	v_pk_mul_f32 v[70:71], v[64:65], v[70:71]
	s_movk_i32 s15, 0x4000
	v_pk_mul_f32 v[76:77], v[156:157], v[76:77]
	v_pk_mul_f32 v[80:81], v[158:159], v[72:73]
	v_cvt_pk_bf16_f32 v72, v74, v75
	v_cvt_pk_bf16_f32 v73, v76, v77
	v_cvt_pk_bf16_f32 v74, v70, v71
	v_add_co_u32_e32 v70, vcc, s15, v162
	v_pk_mul_f32 v[58:59], v[78:79], v[58:59] op_sel_hi:[0,1]
	s_nop 0
	v_addc_co_u32_e32 v71, vcc, 0, v163, vcc
	v_pk_mul_f32 v[56:57], v[78:79], v[56:57] op_sel_hi:[0,1]
	v_pk_mul_f32 v[54:55], v[78:79], v[54:55] op_sel_hi:[0,1]
	v_cvt_pk_bf16_f32 v75, v80, v81
	global_store_dwordx4 v[70:71], v[72:75], off nt
	v_pk_mul_f32 v[60:61], v[78:79], v[60:61] op_sel_hi:[0,1]
	v_pk_mul_f32 v[58:59], v[66:67], v[58:59]
	v_pk_mul_f32 v[72:73], v[160:161], v[56:57]
	v_pk_mul_f32 v[56:57], v[52:53], v[54:55]
	v_cvt_pk_bf16_f32 v54, v58, v59
	v_pk_mul_f32 v[60:61], v[68:69], v[60:61]
	s_and_b64 vcc, exec, s[6:7]
	v_cvt_pk_bf16_f32 v55, v60, v61
	v_cvt_pk_bf16_f32 v56, v56, v57
	v_cvt_pk_bf16_f32 v57, v72, v73
	global_store_dwordx4 v[70:71], v[54:57], off offset:64 nt
	s_nop 1
	v_mov_b32_e32 v54, 1.0
	s_cbranch_vccz .LBB0_269
	s_and_b64 vcc, exec, s[8:9]
	s_mov_b64 s[22:23], -1
	s_cbranch_vccnz .LBB0_270

; __device__ __forceinline__ unsigned cvt_pk_bf16(float lo, float hi) { unsigned r; asm volatile("v_cvt_pk_bf16_f32 %0, %1, %2" : "=v"(r) : "v"(lo), "v"(hi)); return r; }
;     __device__ __forceinline__ void operator()(const f32x4 (&acc)[2][2][4][2], const pg8::Unit& u, int wr, int wc, int fr, int fq) const {
;     ...
;                 bf16_t* rowp = base + (size_t)(ai * 128 + m * 16) * 64;
; #pragma unroll
;                 for (int bj = 0; bj < 2; ++bj) {
;                     const f32x4 v0 = v[bj][0] * rstd * g[bj][0], v1 = v[bj][1] * rstd * g[bj][1];
;                     u32x4 w; w.x = pg8::cvt_pk_bf16(v0[0], v0[1]); w.y = pg8::cvt_pk_bf16(v0[2], v0[3]); w.z = pg8::cvt_pk_bf16(v1[0], v1[1]); w.w = pg8::cvt_pk_bf16(v1[2], v1[3]);
;                     *(u32x4*)(rowp + 32 * bj) = w;
;                 }
.LBB0_272:
	v_pk_mul_f32 v[50:51], v[54:55], v[50:51] op_sel_hi:[0,1]
	v_pk_mul_f32 v[48:49], v[54:55], v[48:49] op_sel_hi:[0,1]
	v_pk_mul_f32 v[46:47], v[54:55], v[46:47] op_sel_hi:[0,1]
	v_pk_mul_f32 v[44:45], v[54:55], v[44:45] op_sel_hi:[0,1]
	v_pk_mul_f32 v[50:51], v[156:157], v[50:51]
	v_pk_mul_f32 v[48:49], v[62:63], v[48:49]
	v_pk_mul_f32 v[56:57], v[158:159], v[46:47]
	v_pk_mul_f32 v[46:47], v[64:65], v[44:45]
	v_cvt_pk_bf16_f32 v44, v48, v49
	v_cvt_pk_bf16_f32 v45, v50, v51
	v_pk_mul_f32 v[40:41], v[54:55], v[40:41] op_sel_hi:[0,1]
	v_pk_mul_f32 v[38:39], v[54:55], v[38:39] op_sel_hi:[0,1]
	v_pk_mul_f32 v[36:37], v[54:55], v[36:37] op_sel_hi:[0,1]
	v_cvt_pk_bf16_f32 v46, v46, v47
	v_cvt_pk_bf16_f32 v47, v56, v57
	global_store_dwordx4 v[70:71], v[44:47], off offset:2048 nt
	v_pk_mul_f32 v[42:43], v[54:55], v[42:43] op_sel_hi:[0,1]
	v_pk_mul_f32 v[40:41], v[66:67], v[40:41]
	v_pk_mul_f32 v[44:45], v[160:161], v[38:39]
	v_pk_mul_f32 v[38:39], v[52:53], v[36:37]
	v_cvt_pk_bf16_f32 v36, v40, v41
	v_pk_mul_f32 v[42:43], v[68:69], v[42:43]
	s_and_b64 vcc, exec, s[6:7]
	v_cvt_pk_bf16_f32 v37, v42, v43
	v_cvt_pk_bf16_f32 v38, v38, v39
	v_cvt_pk_bf16_f32 v39, v44, v45
	global_store_dwordx4 v[70:71], v[36:39], off offset:2112 nt
	s_nop 1
	v_mov_b32_e32 v36, 1.0
	s_cbranch_vccz .LBB0_275
	s_and_b64 vcc, exec, s[8:9]
	s_mov_b64 s[22:23], -1
	s_cbranch_vccnz .LBB0_276

; __device__ __forceinline__ unsigned cvt_pk_bf16(float lo, float hi) { unsigned r; asm volatile("v_cvt_pk_bf16_f32 %0, %1, %2" : "=v"(r) : "v"(lo), "v"(hi)); return r; }
;     __device__ __forceinline__ void operator()(const f32x4 (&acc)[2][2][4][2], const pg8::Unit& u, int wr, int wc, int fr, int fq) const {
;     ...
;                 bf16_t* rowp = base + (size_t)(ai * 128 + m * 16) * 64;
; #pragma unroll
;                 for (int bj = 0; bj < 2; ++bj) {
;                     const f32x4 v0 = v[bj][0] * rstd * g[bj][0], v1 = v[bj][1] * rstd * g[bj][1];
;                     u32x4 w; w.x = pg8::cvt_pk_bf16(v0[0], v0[1]); w.y = pg8::cvt_pk_bf16(v0[2], v0[3]); w.z = pg8::cvt_pk_bf16(v1[0], v1[1]); w.w = pg8::cvt_pk_bf16(v1[2], v1[3]);
;                     *(u32x4*)(rowp + 32 * bj) = w;
;                 }
.LBB0_278:
	v_pk_mul_f32 v[30:31], v[36:37], v[30:31] op_sel_hi:[0,1]
	v_pk_mul_f32 v[26:27], v[36:37], v[26:27] op_sel_hi:[0,1]
	v_pk_mul_f32 v[32:33], v[36:37], v[32:33] op_sel_hi:[0,1]
	v_pk_mul_f32 v[30:31], v[62:63], v[30:31]
	v_pk_mul_f32 v[28:29], v[36:37], v[28:29] op_sel_hi:[0,1]
	v_pk_mul_f32 v[26:27], v[64:65], v[26:27]
	s_movk_i32 s15, 0x5000
	v_pk_mul_f32 v[32:33], v[156:157], v[32:33]
	v_pk_mul_f32 v[38:39], v[158:159], v[28:29]
	v_cvt_pk_bf16_f32 v28, v30, v31
	v_cvt_pk_bf16_f32 v29, v32, v33
	v_cvt_pk_bf16_f32 v30, v26, v27
	v_add_co_u32_e32 v26, vcc, s15, v162
	v_pk_mul_f32 v[22:23], v[36:37], v[22:23] op_sel_hi:[0,1]
	s_nop 0
	v_addc_co_u32_e32 v27, vcc, 0, v163, vcc
	v_pk_mul_f32 v[20:21], v[36:37], v[20:21] op_sel_hi:[0,1]
	v_pk_mul_f32 v[18:19], v[36:37], v[18:19] op_sel_hi:[0,1]
	v_cvt_pk_bf16_f32 v31, v38, v39
	global_store_dwordx4 v[26:27], v[28:31], off nt
	v_pk_mul_f32 v[24:25], v[36:37], v[24:25] op_sel_hi:[0,1]
	v_pk_mul_f32 v[22:23], v[66:67], v[22:23]
	v_pk_mul_f32 v[28:29], v[160:161], v[20:21]
	v_pk_mul_f32 v[20:21], v[52:53], v[18:19]
	v_cvt_pk_bf16_f32 v18, v22, v23
	v_pk_mul_f32 v[24:25], v[68:69], v[24:25]
	s_and_b64 vcc, exec, s[6:7]
	v_cvt_pk_bf16_f32 v19, v24, v25
	v_cvt_pk_bf16_f32 v20, v20, v21
	v_cvt_pk_bf16_f32 v21, v28, v29
	global_store_dwordx4 v[26:27], v[18:21], off offset:64 nt
	s_nop 1
	v_mov_b32_e32 v18, 1.0
	s_cbranch_vccz .LBB0_281
	s_and_b64 vcc, exec, s[8:9]
	s_mov_b64 s[6:7], -1
	s_cbranch_vccnz .LBB0_282

; __device__ __forceinline__ unsigned cvt_pk_bf16(float lo, float hi) { unsigned r; asm volatile("v_cvt_pk_bf16_f32 %0, %1, %2" : "=v"(r) : "v"(lo), "v"(hi)); return r; }
;     __device__ __forceinline__ void operator()(const f32x4 (&acc)[2][2][4][2], const pg8::Unit& u, int wr, int wc, int fr, int fq) const {
;     ...
;                 bf16_t* rowp = base + (size_t)(ai * 128 + m * 16) * 64;
; #pragma unroll
;                 for (int bj = 0; bj < 2; ++bj) {
;                     const f32x4 v0 = v[bj][0] * rstd * g[bj][0], v1 = v[bj][1] * rstd * g[bj][1];
;                     u32x4 w; w.x = pg8::cvt_pk_bf16(v0[0], v0[1]); w.y = pg8::cvt_pk_bf16(v0[2], v0[3]); w.z = pg8::cvt_pk_bf16(v1[0], v1[1]); w.w = pg8::cvt_pk_bf16(v1[2], v1[3]);
;                     *(u32x4*)(rowp + 32 * bj) = w;
;                 }
.LBB0_284:
	v_pk_mul_f32 v[16:17], v[18:19], v[16:17] op_sel_hi:[0,1]
	v_pk_mul_f32 v[14:15], v[18:19], v[14:15] op_sel_hi:[0,1]
	v_pk_mul_f32 v[12:13], v[18:19], v[12:13] op_sel_hi:[0,1]
	v_pk_mul_f32 v[10:11], v[18:19], v[10:11] op_sel_hi:[0,1]
	v_pk_mul_f32 v[16:17], v[156:157], v[16:17]
	v_pk_mul_f32 v[14:15], v[62:63], v[14:15]
	v_pk_mul_f32 v[20:21], v[158:159], v[12:13]
	v_pk_mul_f32 v[12:13], v[64:65], v[10:11]
	v_cvt_pk_bf16_f32 v10, v14, v15
	v_cvt_pk_bf16_f32 v11, v16, v17
	v_pk_mul_f32 v[4:5], v[18:19], v[4:5] op_sel_hi:[0,1]
	v_pk_mul_f32 v[2:3], v[18:19], v[2:3] op_sel_hi:[0,1]
	v_cvt_pk_bf16_f32 v12, v12, v13
	v_cvt_pk_bf16_f32 v13, v20, v21
	global_store_dwordx4 v[26:27], v[10:13], off offset:2048 nt
	v_pk_mul_f32 v[8:9], v[18:19], v[8:9] op_sel_hi:[0,1]
	v_pk_mul_f32 v[6:7], v[18:19], v[6:7] op_sel_hi:[0,1]
	v_pk_mul_f32 v[10:11], v[160:161], v[4:5]
	v_pk_mul_f32 v[4:5], v[52:53], v[2:3]
	s_andn2_b64 vcc, exec, s[4:5]
	s_mov_b64 s[4:5], -1
	v_pk_mul_f32 v[8:9], v[68:69], v[8:9]
	v_pk_mul_f32 v[6:7], v[66:67], v[6:7]
	s_nop 0
	v_cvt_pk_bf16_f32 v2, v6, v7
	v_cvt_pk_bf16_f32 v3, v8, v9
	v_cvt_pk_bf16_f32 v4, v4, v5
	v_cvt_pk_bf16_f32 v5, v10, v11
	global_store_dwordx4 v[26:27], v[2:5], off offset:2112 nt
	s_cbranch_vccnz .LBB0_209
	s_andn2_b64 vcc, exec, s[10:11]
	s_cbranch_vccnz .LBB0_208
	s_barrier
	s_branch .LBB0_208

; __device__ __forceinline__ void cumsum_unit(const Args& a, LAS unsigned char* lds, int bh) {
;     ...
;     double base = incl - run;
;     for (int w = 0; w < (tid >> 6); ++w) base += sd[w];
; #pragma unroll
;     for (int j = 0; j < 8; ++j) cum[tid * 8 + j] = (float)(base + loc[j]);
;     __syncthreads();
.LBB0_301:
	s_or_b64 exec, exec, s[4:5]
	v_readlane_b32 s4, v252, 34
	v_readlane_b32 s5, v252, 35
	v_add_f64 v[22:23], v[16:17], v[20:21]
	v_add_f64 v[16:17], v[18:19], v[20:21]
	v_lshl_add_u64 v[24:25], v[2:3], 2, s[4:5]
	v_add_f64 v[2:3], v[12:13], v[20:21]
	v_cvt_f32_f64_e32 v18, v[2:3]
	v_add_f64 v[4:5], v[4:5], v[20:21]
	v_add_f64 v[2:3], v[6:7], v[20:21]
	v_add_f64 v[12:13], v[14:15], v[20:21]
	v_cvt_f32_f64_e32 v3, v[2:3]
	v_cvt_f32_f64_e32 v2, v[4:5]
	v_add_f64 v[6:7], v[8:9], v[20:21]
	v_add_f64 v[4:5], v[10:11], v[20:21]
	v_cvt_f32_f64_e32 v17, v[16:17]
	v_cvt_f32_f64_e32 v16, v[22:23]
	v_cvt_f32_f64_e32 v19, v[12:13]
	v_cvt_f32_f64_e32 v5, v[4:5]
	v_cvt_f32_f64_e32 v4, v[6:7]
	global_store_dwordx4 v[24:25], v[16:19], off nt
	global_store_dwordx4 v[24:25], v[2:5], off offset:16 nt
	s_barrier

; #define LAS __attribute__((address_space(3)))
; __device__ __forceinline__ unsigned pk2(float lo, float hi) { pk2_f32x2 v = {lo, hi}; pk2_bf16x2 b = __builtin_convertvector(v, pk2_bf16x2); return __builtin_bit_cast(unsigned, b); }
;     ...
;         asm volatile("s_waitcnt lgkmcnt(0)" ::: "memory");
;         const int c = lane & 7;
; #pragma unroll
;         for (int j = 0; j < 4; ++j) { const int n = (lane >> 3) + 8 * j; const LAS float* sp = scr + (8 * c) * 33 + n;
;             u32x4 o; o.x = pk2(sp[0 * 33], sp[1 * 33]); o.y = pk2(sp[2 * 33], sp[3 * 33]); o.z = pk2(sp[4 * 33], sp[5 * 33]); o.w = pk2(sp[6 * 33], sp[7 * 33]);
;             *(u32x4*)(p.dst + (size_t)n * p.K + 8 * c) = o; }
;         asm volatile("s_waitcnt lgkmcnt(0)" ::: "memory");
.LBB0_319:
	s_or_b64 exec, exec, s[10:11]
	v_mov_b32_e32 v37, v35
	s_waitcnt lgkmcnt(0)
	v_lshl_add_u64 v[46:47], v[42:43], 0, v[36:37]
	v_add_u32_e32 v37, 0xc000, v80
	ds_read2_b32 v[94:95], v37 offset0:33 offset1:41
	ds_read2_b32 v[96:97], v37 offset1:8
	ds_read2_b32 v[98:99], v37 offset0:66 offset1:74
	ds_read2_b32 v[100:101], v37 offset0:99 offset1:107
	ds_read2_b32 v[102:103], v37 offset0:132 offset1:140
	ds_read2_b32 v[104:105], v37 offset0:165 offset1:173
	ds_read2_b32 v[106:107], v37 offset0:198 offset1:206
	ds_read2_b32 v[108:109], v37 offset0:231 offset1:239
	v_mul_u32_u24_e32 v39, v38, v79
	v_lshlrev_b32_e32 v110, 1, v39
	v_mov_b32_e32 v111, v35
	s_waitcnt lgkmcnt(6)
	v_cvt_pk_bf16_f32 v42, v96, v94
	s_waitcnt lgkmcnt(4)
	v_cvt_pk_bf16_f32 v43, v98, v100
	s_waitcnt lgkmcnt(2)
	v_cvt_pk_bf16_f32 v44, v102, v104
	s_waitcnt lgkmcnt(0)
	v_cvt_pk_bf16_f32 v45, v106, v108
	v_lshl_add_u64 v[110:111], v[46:47], 0, v[110:111]
	v_mul_u32_u24_e32 v39, v38, v81
	global_store_dwordx4 v[110:111], v[42:45], off nt
	v_lshlrev_b32_e32 v94, 1, v39
	v_mov_b32_e32 v111, v35
	v_cvt_pk_bf16_f32 v42, v97, v95
	v_mov_b32_e32 v95, v35
	v_cvt_pk_bf16_f32 v43, v99, v101
	v_cvt_pk_bf16_f32 v44, v103, v105
	v_cvt_pk_bf16_f32 v45, v107, v109
	v_lshl_add_u64 v[94:95], v[46:47], 0, v[94:95]
	global_store_dwordx4 v[94:95], v[42:45], off nt
	ds_read2_b32 v[94:95], v37 offset0:16 offset1:24
	ds_read2_b32 v[96:97], v37 offset0:49 offset1:57
	ds_read2_b32 v[98:99], v37 offset0:82 offset1:90
	ds_read2_b32 v[100:101], v37 offset0:115 offset1:123
	ds_read2_b32 v[102:103], v37 offset0:148 offset1:156
	ds_read2_b32 v[104:105], v37 offset0:181 offset1:189
	ds_read2_b32 v[106:107], v37 offset0:214 offset1:222
	ds_read2_b32 v[108:109], v37 offset0:247 offset1:255
	v_mul_u32_u24_e32 v37, v38, v82
	v_lshlrev_b32_e32 v110, 1, v37
	v_mul_u32_u24_e32 v37, v38, v83
	s_waitcnt lgkmcnt(6)
	v_cvt_pk_bf16_f32 v42, v94, v96
	s_waitcnt lgkmcnt(4)
	v_cvt_pk_bf16_f32 v43, v98, v100
	s_waitcnt lgkmcnt(2)
	v_cvt_pk_bf16_f32 v44, v102, v104
	s_waitcnt lgkmcnt(0)
	v_cvt_pk_bf16_f32 v45, v106, v108
	v_lshl_add_u64 v[110:111], v[46:47], 0, v[110:111]
	v_lshlrev_b32_e32 v38, 1, v37
	v_mov_b32_e32 v39, v35
	global_store_dwordx4 v[110:111], v[42:45], off nt
	v_lshl_add_u64 v[38:39], v[46:47], 0, v[38:39]
	s_and_b64 s[4:5], exec, vcc
	v_cvt_pk_bf16_f32 v42, v95, v97
	v_cvt_pk_bf16_f32 v43, v99, v101
	v_cvt_pk_bf16_f32 v44, v103, v105
	v_cvt_pk_bf16_f32 v45, v107, v109
	global_store_dwordx4 v[38:39], v[42:45], off nt
	s_waitcnt lgkmcnt(0)
	s_or_b64 s[8:9], s[4:5], s[8:9]
	v_add_u32_e32 v84, s2, v84
	v_add_u32_e32 v85, s18, v85
	v_add_u32_e32 v86, s19, v86
	v_add_u32_e32 v87, s20, v87
	v_add_u32_e32 v88, s21, v88
	v_add_u32_e32 v89, s22, v89
	v_add_u32_e32 v90, s23, v90
	v_add_u32_e32 v91, s24, v91
	v_mov_b32_e32 v37, v40
	s_andn2_b64 exec, exec, s[8:9]
	s_cbranch_execz .LBB0_345

; __device__ __forceinline__ unsigned cvt_pk_bf16(float lo, float hi) { unsigned r; asm volatile("v_cvt_pk_bf16_f32 %0, %1, %2" : "=v"(r) : "v"(lo), "v"(hi)); return r; }
;     __device__ __forceinline__ void operator()(const f32x4 (&acc)[2][2][4][2], const pg8::Unit& u, int wr, int wc, int fr, int fq) const {
;     ...
;                 const int ll = ai * 128 + wr * 64 + m * 16 + fr, lr = u.pm * 256 + ll;
;                 if (lr < cnt) {
;                     const int ent = sl_e[ll]; const float gw = sl_g[ll];
;                     bf16_t* rowp = yb + ((size_t)(ent & 1) * NTOK + (size_t)(ent >> 1)) * D + col0;
; #pragma unroll
;                     for (int bj = 0; bj < 2; ++bj) {
;                         const f32x4 v0 = acc[ai][bj][m][0] * gw, v1 = acc[ai][bj][m][1] * gw;
;                         u32x4 w; w.x = pg8::cvt_pk_bf16(v0[0], v0[1]); w.y = pg8::cvt_pk_bf16(v0[2], v0[3]); w.z = pg8::cvt_pk_bf16(v1[0], v1[1]); w.w = pg8::cvt_pk_bf16(v1[2], v1[3]);
;                         *(u32x4*)(rowp + bj * 128) = w;
;                     }
.LBB0_1300:
	s_lshl_b32 s6, s10, 2
	s_add_i32 s6, s6, 0
	s_add_i32 s6, s6, 0x21e00
	v_mov_b32_e32 v34, s6
	ds_read_b32 v134, v34
	v_lshl_or_b32 v36, s12, 8, v244
	s_add_i32 s54, s54, 0x22400
	v_add_u32_e32 v136, s22, v226
	v_ashrrev_i32_e32 v37, 31, v36
	s_waitcnt lgkmcnt(0)
	v_cmp_lt_i32_e32 vcc, v136, v134
	v_lshl_add_u32 v135, v226, 2, s54
	s_and_saveexec_b64 s[6:7], vcc
	s_cbranch_execz .LBB0_1302
	ds_read2st64_b32 v[138:139], v135 offset1:4
	s_waitcnt lgkmcnt(0)
	v_lshlrev_b32_e32 v34, 15, v138
	v_ashrrev_i32_e32 v138, 1, v138
	v_mov_b32_e32 v142, v139
	v_and_b32_e32 v34, 0x8000, v34
	v_ashrrev_i32_e32 v139, 31, v138
	v_lshl_add_u64 v[138:139], v[34:35], 0, v[138:139]
	v_lshlrev_b64 v[138:139], 11, v[138:139]
	v_lshl_add_u64 v[138:139], s[96:97], 0, v[138:139]
	v_pk_mul_f32 v[140:141], v[132:133], v[142:143] op_sel_hi:[1,0]
	v_lshl_add_u64 v[144:145], v[36:37], 1, v[138:139]
	v_pk_mul_f32 v[138:139], v[130:131], v[142:143] op_sel_hi:[1,0]
	v_pk_mul_f32 v[146:147], v[128:129], v[142:143] op_sel_hi:[1,0]
	v_pk_mul_f32 v[148:149], v[126:127], v[142:143] op_sel_hi:[1,0]
	v_cvt_pk_bf16_f32 v138, v138, v139
	v_cvt_pk_bf16_f32 v139, v140, v141
	s_nop 0
	v_cvt_pk_bf16_f32 v140, v148, v149
	v_cvt_pk_bf16_f32 v141, v146, v147
	global_store_dwordx4 v[144:145], v[138:141], off nt
	v_pk_mul_f32 v[146:147], v[96:97], v[142:143] op_sel_hi:[1,0]
	s_nop 0
	v_pk_mul_f32 v[140:141], v[100:101], v[142:143] op_sel_hi:[1,0]
	v_pk_mul_f32 v[138:139], v[98:99], v[142:143] op_sel_hi:[1,0]
	v_pk_mul_f32 v[142:143], v[94:95], v[142:143] op_sel_hi:[1,0]
	v_cvt_pk_bf16_f32 v138, v138, v139
	v_cvt_pk_bf16_f32 v139, v140, v141
	s_nop 0
	v_cvt_pk_bf16_f32 v140, v142, v143
	v_cvt_pk_bf16_f32 v141, v146, v147
	global_store_dwordx4 v[144:145], v[138:141], off offset:256 nt
.LBB0_1302:
	s_or_b64 exec, exec, s[6:7]
	v_add_u32_e32 v34, s22, v228
	v_cmp_lt_i32_e32 vcc, v34, v134
	s_and_saveexec_b64 s[6:7], vcc
	s_cbranch_execz .LBB0_1304
	v_add_u32_e32 v34, 64, v135
	ds_read2st64_b32 v[138:139], v34 offset1:4
	s_waitcnt lgkmcnt(0)
	v_lshlrev_b32_e32 v34, 15, v138
	v_ashrrev_i32_e32 v138, 1, v138
	v_mov_b32_e32 v142, v139
	v_and_b32_e32 v34, 0x8000, v34
	v_ashrrev_i32_e32 v139, 31, v138
	v_lshl_add_u64 v[138:139], v[34:35], 0, v[138:139]
	v_lshlrev_b64 v[138:139], 11, v[138:139]
	v_lshl_add_u64 v[138:139], s[96:97], 0, v[138:139]
	v_pk_mul_f32 v[140:141], v[124:125], v[142:143] op_sel_hi:[1,0]
	v_lshl_add_u64 v[144:145], v[36:37], 1, v[138:139]
	v_pk_mul_f32 v[138:139], v[122:123], v[142:143] op_sel_hi:[1,0]
	v_pk_mul_f32 v[146:147], v[120:121], v[142:143] op_sel_hi:[1,0]
	v_pk_mul_f32 v[148:149], v[118:119], v[142:143] op_sel_hi:[1,0]
	v_cvt_pk_bf16_f32 v138, v138, v139
	v_cvt_pk_bf16_f32 v139, v140, v141
	s_nop 0
	v_cvt_pk_bf16_f32 v140, v148, v149
	v_cvt_pk_bf16_f32 v141, v146, v147
	global_store_dwordx4 v[144:145], v[138:141], off nt
	v_pk_mul_f32 v[146:147], v[88:89], v[142:143] op_sel_hi:[1,0]
	s_nop 0
	v_pk_mul_f32 v[140:141], v[92:93], v[142:143] op_sel_hi:[1,0]
	v_pk_mul_f32 v[138:139], v[90:91], v[142:143] op_sel_hi:[1,0]
	v_pk_mul_f32 v[142:143], v[86:87], v[142:143] op_sel_hi:[1,0]
	v_cvt_pk_bf16_f32 v138, v138, v139
	v_cvt_pk_bf16_f32 v139, v140, v141
	s_nop 0
	v_cvt_pk_bf16_f32 v140, v142, v143
	v_cvt_pk_bf16_f32 v141, v146, v147
	global_store_dwordx4 v[144:145], v[138:141], off offset:256 nt
.LBB0_1304:
	s_or_b64 exec, exec, s[6:7]
	v_add_u32_e32 v34, s22, v229
	v_cmp_lt_i32_e32 vcc, v34, v134
	s_and_saveexec_b64 s[6:7], vcc
	s_cbranch_execz .LBB0_1306
	v_add_u32_e32 v34, 0x80, v135
	ds_read2st64_b32 v[138:139], v34 offset1:4
	s_waitcnt lgkmcnt(0)
	v_lshlrev_b32_e32 v34, 15, v138
	v_ashrrev_i32_e32 v138, 1, v138
	v_mov_b32_e32 v142, v139
	v_and_b32_e32 v34, 0x8000, v34
	v_ashrrev_i32_e32 v139, 31, v138
	v_lshl_add_u64 v[138:139], v[34:35], 0, v[138:139]
	v_lshlrev_b64 v[138:139], 11, v[138:139]
	v_lshl_add_u64 v[138:139], s[96:97], 0, v[138:139]
	v_pk_mul_f32 v[140:141], v[116:117], v[142:143] op_sel_hi:[1,0]
	v_lshl_add_u64 v[144:145], v[36:37], 1, v[138:139]
	v_pk_mul_f32 v[138:139], v[114:115], v[142:143] op_sel_hi:[1,0]
	v_pk_mul_f32 v[146:147], v[112:113], v[142:143] op_sel_hi:[1,0]
	v_pk_mul_f32 v[148:149], v[110:111], v[142:143] op_sel_hi:[1,0]
	v_cvt_pk_bf16_f32 v138, v138, v139
	v_cvt_pk_bf16_f32 v139, v140, v141
	s_nop 0
	v_cvt_pk_bf16_f32 v140, v148, v149
	v_cvt_pk_bf16_f32 v141, v146, v147
	global_store_dwordx4 v[144:145], v[138:141], off nt
	v_pk_mul_f32 v[146:147], v[80:81], v[142:143] op_sel_hi:[1,0]
	s_nop 0
	v_pk_mul_f32 v[140:141], v[84:85], v[142:143] op_sel_hi:[1,0]
	v_pk_mul_f32 v[138:139], v[82:83], v[142:143] op_sel_hi:[1,0]
	v_pk_mul_f32 v[142:143], v[78:79], v[142:143] op_sel_hi:[1,0]
	v_cvt_pk_bf16_f32 v138, v138, v139
	v_cvt_pk_bf16_f32 v139, v140, v141
	s_nop 0
	v_cvt_pk_bf16_f32 v140, v142, v143
	v_cvt_pk_bf16_f32 v141, v146, v147
	global_store_dwordx4 v[144:145], v[138:141], off offset:256 nt
; __device__ __forceinline__ unsigned cvt_pk_bf16(float lo, float hi) { unsigned r; asm volatile("v_cvt_pk_bf16_f32 %0, %1, %2" : "=v"(r) : "v"(lo), "v"(hi)); return r; }
;     __device__ __forceinline__ void operator()(const f32x4 (&acc)[2][2][4][2], const pg8::Unit& u, int wr, int wc, int fr, int fq) const {
;     ...
;                 const int ll = ai * 128 + wr * 64 + m * 16 + fr, lr = u.pm * 256 + ll;
;                 if (lr < cnt) {
;                     const int ent = sl_e[ll]; const float gw = sl_g[ll];
;                     bf16_t* rowp = yb + ((size_t)(ent & 1) * NTOK + (size_t)(ent >> 1)) * D + col0;
; #pragma unroll
;                     for (int bj = 0; bj < 2; ++bj) {
;                         const f32x4 v0 = acc[ai][bj][m][0] * gw, v1 = acc[ai][bj][m][1] * gw;
;                         u32x4 w; w.x = pg8::cvt_pk_bf16(v0[0], v0[1]); w.y = pg8::cvt_pk_bf16(v0[2], v0[3]); w.z = pg8::cvt_pk_bf16(v1[0], v1[1]); w.w = pg8::cvt_pk_bf16(v1[2], v1[3]);
;                         *(u32x4*)(rowp + bj * 128) = w;
;                     }
.LBB0_1306:
	s_or_b64 exec, exec, s[6:7]
	v_add_u32_e32 v34, s22, v243
	v_cmp_lt_i32_e32 vcc, v34, v134
	s_and_saveexec_b64 s[6:7], vcc
	s_cbranch_execz .LBB0_1308
	v_add_u32_e32 v34, 0xc0, v135
	ds_read2st64_b32 v[138:139], v34 offset1:4
	s_waitcnt lgkmcnt(0)
	v_lshlrev_b32_e32 v34, 15, v138
	v_ashrrev_i32_e32 v138, 1, v138
	v_mov_b32_e32 v142, v139
	v_and_b32_e32 v34, 0x8000, v34
	v_ashrrev_i32_e32 v139, 31, v138
	v_lshl_add_u64 v[138:139], v[34:35], 0, v[138:139]
	v_lshlrev_b64 v[138:139], 11, v[138:139]
	v_lshl_add_u64 v[138:139], s[96:97], 0, v[138:139]
	v_pk_mul_f32 v[140:141], v[108:109], v[142:143] op_sel_hi:[1,0]
	v_lshl_add_u64 v[144:145], v[36:37], 1, v[138:139]
	v_pk_mul_f32 v[138:139], v[106:107], v[142:143] op_sel_hi:[1,0]
	v_pk_mul_f32 v[146:147], v[104:105], v[142:143] op_sel_hi:[1,0]
	v_pk_mul_f32 v[148:149], v[102:103], v[142:143] op_sel_hi:[1,0]
	v_cvt_pk_bf16_f32 v138, v138, v139
	v_cvt_pk_bf16_f32 v139, v140, v141
	s_nop 0
	v_cvt_pk_bf16_f32 v140, v148, v149
	v_cvt_pk_bf16_f32 v141, v146, v147
	global_store_dwordx4 v[144:145], v[138:141], off nt
	v_pk_mul_f32 v[146:147], v[72:73], v[142:143] op_sel_hi:[1,0]
	s_nop 0
	v_pk_mul_f32 v[140:141], v[76:77], v[142:143] op_sel_hi:[1,0]
	v_pk_mul_f32 v[138:139], v[74:75], v[142:143] op_sel_hi:[1,0]
	v_pk_mul_f32 v[142:143], v[70:71], v[142:143] op_sel_hi:[1,0]
	v_cvt_pk_bf16_f32 v138, v138, v139
	v_cvt_pk_bf16_f32 v139, v140, v141
	s_nop 0
	v_cvt_pk_bf16_f32 v140, v142, v143
	v_cvt_pk_bf16_f32 v141, v146, v147
	global_store_dwordx4 v[144:145], v[138:141], off offset:256 nt
.LBB0_1308:
	s_or_b64 exec, exec, s[6:7]
	v_add_u32_e32 v34, 0x80, v136
	v_cmp_lt_i32_e32 vcc, v34, v134
	s_and_saveexec_b64 s[6:7], vcc
	s_cbranch_execz .LBB0_1310
	ds_read2st64_b32 v[138:139], v135 offset0:2 offset1:6
	s_waitcnt lgkmcnt(0)
	v_lshlrev_b32_e32 v34, 15, v138
	v_ashrrev_i32_e32 v138, 1, v138
	v_mov_b32_e32 v142, v139
	v_and_b32_e32 v34, 0x8000, v34
	v_ashrrev_i32_e32 v139, 31, v138
	v_lshl_add_u64 v[138:139], v[34:35], 0, v[138:139]
	v_lshlrev_b64 v[138:139], 11, v[138:139]
	v_lshl_add_u64 v[138:139], s[96:97], 0, v[138:139]
	v_pk_mul_f32 v[140:141], v[68:69], v[142:143] op_sel_hi:[1,0]
	v_lshl_add_u64 v[144:145], v[36:37], 1, v[138:139]
	v_pk_mul_f32 v[138:139], v[66:67], v[142:143] op_sel_hi:[1,0]
	v_pk_mul_f32 v[146:147], v[64:65], v[142:143] op_sel_hi:[1,0]
	v_pk_mul_f32 v[148:149], v[62:63], v[142:143] op_sel_hi:[1,0]
	v_cvt_pk_bf16_f32 v138, v138, v139
	v_cvt_pk_bf16_f32 v139, v140, v141
	s_nop 0
	v_cvt_pk_bf16_f32 v140, v148, v149
	v_cvt_pk_bf16_f32 v141, v146, v147
	global_store_dwordx4 v[144:145], v[138:141], off nt
	v_pk_mul_f32 v[146:147], v[28:29], v[142:143] op_sel_hi:[1,0]
	s_nop 0
	v_pk_mul_f32 v[140:141], v[32:33], v[142:143] op_sel_hi:[1,0]
	v_pk_mul_f32 v[138:139], v[30:31], v[142:143] op_sel_hi:[1,0]
	v_pk_mul_f32 v[142:143], v[26:27], v[142:143] op_sel_hi:[1,0]
	v_cvt_pk_bf16_f32 v138, v138, v139
	v_cvt_pk_bf16_f32 v139, v140, v141
	s_nop 0
	v_cvt_pk_bf16_f32 v140, v142, v143
	v_cvt_pk_bf16_f32 v141, v146, v147
	global_store_dwordx4 v[144:145], v[138:141], off offset:256 nt
.LBB0_1310:
	s_or_b64 exec, exec, s[6:7]
	v_add_u32_e32 v34, 0x90, v136
	v_cmp_lt_i32_e32 vcc, v34, v134
	s_and_saveexec_b64 s[6:7], vcc
	s_cbranch_execz .LBB0_1312
	v_add_u32_e32 v34, 64, v135
	ds_read2st64_b32 v[138:139], v34 offset0:2 offset1:6
	s_waitcnt lgkmcnt(0)
	v_lshlrev_b32_e32 v34, 15, v138
	v_ashrrev_i32_e32 v138, 1, v138
	v_mov_b32_e32 v142, v139
	v_and_b32_e32 v34, 0x8000, v34
	v_ashrrev_i32_e32 v139, 31, v138
	v_lshl_add_u64 v[138:139], v[34:35], 0, v[138:139]
	v_lshlrev_b64 v[138:139], 11, v[138:139]
	v_lshl_add_u64 v[138:139], s[96:97], 0, v[138:139]
	v_pk_mul_f32 v[140:141], v[60:61], v[142:143] op_sel_hi:[1,0]
	v_lshl_add_u64 v[144:145], v[36:37], 1, v[138:139]
	v_pk_mul_f32 v[138:139], v[58:59], v[142:143] op_sel_hi:[1,0]
	v_pk_mul_f32 v[146:147], v[56:57], v[142:143] op_sel_hi:[1,0]
	v_pk_mul_f32 v[148:149], v[54:55], v[142:143] op_sel_hi:[1,0]
	v_cvt_pk_bf16_f32 v138, v138, v139
	v_cvt_pk_bf16_f32 v139, v140, v141
	s_nop 0
	v_cvt_pk_bf16_f32 v140, v148, v149
	v_cvt_pk_bf16_f32 v141, v146, v147
	global_store_dwordx4 v[144:145], v[138:141], off nt
	v_pk_mul_f32 v[146:147], v[20:21], v[142:143] op_sel_hi:[1,0]
	s_nop 0
	v_pk_mul_f32 v[140:141], v[24:25], v[142:143] op_sel_hi:[1,0]
	v_pk_mul_f32 v[138:139], v[22:23], v[142:143] op_sel_hi:[1,0]
	v_pk_mul_f32 v[142:143], v[18:19], v[142:143] op_sel_hi:[1,0]
	v_cvt_pk_bf16_f32 v138, v138, v139
	v_cvt_pk_bf16_f32 v139, v140, v141
	s_nop 0
	v_cvt_pk_bf16_f32 v140, v142, v143
	v_cvt_pk_bf16_f32 v141, v146, v147
	global_store_dwordx4 v[144:145], v[138:141], off offset:256 nt
; __device__ __forceinline__ unsigned cvt_pk_bf16(float lo, float hi) { unsigned r; asm volatile("v_cvt_pk_bf16_f32 %0, %1, %2" : "=v"(r) : "v"(lo), "v"(hi)); return r; }
;     __device__ __forceinline__ void operator()(const f32x4 (&acc)[2][2][4][2], const pg8::Unit& u, int wr, int wc, int fr, int fq) const {
;     ...
;                 const int ll = ai * 128 + wr * 64 + m * 16 + fr, lr = u.pm * 256 + ll;
;                 if (lr < cnt) {
;                     const int ent = sl_e[ll]; const float gw = sl_g[ll];
;                     bf16_t* rowp = yb + ((size_t)(ent & 1) * NTOK + (size_t)(ent >> 1)) * D + col0;
; #pragma unroll
;                     for (int bj = 0; bj < 2; ++bj) {
;                         const f32x4 v0 = acc[ai][bj][m][0] * gw, v1 = acc[ai][bj][m][1] * gw;
;                         u32x4 w; w.x = pg8::cvt_pk_bf16(v0[0], v0[1]); w.y = pg8::cvt_pk_bf16(v0[2], v0[3]); w.z = pg8::cvt_pk_bf16(v1[0], v1[1]); w.w = pg8::cvt_pk_bf16(v1[2], v1[3]);
;                         *(u32x4*)(rowp + bj * 128) = w;
;                     }
.LBB0_1312:
	s_or_b64 exec, exec, s[6:7]
	v_add_u32_e32 v34, 0xa0, v136
	v_cmp_lt_i32_e32 vcc, v34, v134
	s_and_saveexec_b64 s[6:7], vcc
	s_cbranch_execz .LBB0_1314
	v_add_u32_e32 v34, 0x80, v135
	ds_read2st64_b32 v[138:139], v34 offset0:2 offset1:6
	s_waitcnt lgkmcnt(0)
	v_lshlrev_b32_e32 v34, 15, v138
	v_ashrrev_i32_e32 v138, 1, v138
	v_mov_b32_e32 v142, v139
	v_and_b32_e32 v34, 0x8000, v34
	v_ashrrev_i32_e32 v139, 31, v138
	v_lshl_add_u64 v[138:139], v[34:35], 0, v[138:139]
	v_lshlrev_b64 v[138:139], 11, v[138:139]
	v_lshl_add_u64 v[138:139], s[96:97], 0, v[138:139]
	v_pk_mul_f32 v[140:141], v[52:53], v[142:143] op_sel_hi:[1,0]
	v_lshl_add_u64 v[144:145], v[36:37], 1, v[138:139]
	v_pk_mul_f32 v[138:139], v[50:51], v[142:143] op_sel_hi:[1,0]
	v_pk_mul_f32 v[146:147], v[48:49], v[142:143] op_sel_hi:[1,0]
	v_pk_mul_f32 v[148:149], v[46:47], v[142:143] op_sel_hi:[1,0]
	v_cvt_pk_bf16_f32 v138, v138, v139
	v_cvt_pk_bf16_f32 v139, v140, v141
	s_nop 0
	v_cvt_pk_bf16_f32 v140, v148, v149
	v_cvt_pk_bf16_f32 v141, v146, v147
	global_store_dwordx4 v[144:145], v[138:141], off nt
	v_pk_mul_f32 v[146:147], v[12:13], v[142:143] op_sel_hi:[1,0]
	s_nop 0
	v_pk_mul_f32 v[140:141], v[16:17], v[142:143] op_sel_hi:[1,0]
	v_pk_mul_f32 v[138:139], v[14:15], v[142:143] op_sel_hi:[1,0]
	v_pk_mul_f32 v[142:143], v[10:11], v[142:143] op_sel_hi:[1,0]
	v_cvt_pk_bf16_f32 v138, v138, v139
	v_cvt_pk_bf16_f32 v139, v140, v141
	s_nop 0
	v_cvt_pk_bf16_f32 v140, v142, v143
	v_cvt_pk_bf16_f32 v141, v146, v147
	global_store_dwordx4 v[144:145], v[138:141], off offset:256 nt
.LBB0_1314:
	s_or_b64 exec, exec, s[6:7]
	v_add_u32_e32 v34, 0xb0, v136
	v_cmp_lt_i32_e32 vcc, v34, v134
	s_and_saveexec_b64 s[6:7], vcc
	s_cbranch_execz .LBB0_1316
	v_add_u32_e32 v34, 0xc0, v135
	ds_read2st64_b32 v[134:135], v34 offset0:2 offset1:6
	s_waitcnt lgkmcnt(0)
	v_lshlrev_b32_e32 v34, 15, v134
	v_ashrrev_i32_e32 v134, 1, v134
	v_mov_b32_e32 v138, v135
	v_and_b32_e32 v34, 0x8000, v34
	v_ashrrev_i32_e32 v135, 31, v134
	v_lshl_add_u64 v[134:135], v[34:35], 0, v[134:135]
	v_lshlrev_b64 v[134:135], 11, v[134:135]
	v_lshl_add_u64 v[134:135], s[96:97], 0, v[134:135]
	v_pk_mul_f32 v[136:137], v[44:45], v[138:139] op_sel_hi:[1,0]
	v_lshl_add_u64 v[36:37], v[36:37], 1, v[134:135]
	v_pk_mul_f32 v[134:135], v[42:43], v[138:139] op_sel_hi:[1,0]
	v_pk_mul_f32 v[140:141], v[40:41], v[138:139] op_sel_hi:[1,0]
	v_pk_mul_f32 v[142:143], v[38:39], v[138:139] op_sel_hi:[1,0]
	v_cvt_pk_bf16_f32 v134, v134, v135
	v_cvt_pk_bf16_f32 v135, v136, v137
	s_nop 0
	v_cvt_pk_bf16_f32 v136, v142, v143
	v_cvt_pk_bf16_f32 v137, v140, v141
	global_store_dwordx4 v[36:37], v[134:137], off nt
	v_pk_mul_f32 v[140:141], v[4:5], v[138:139] op_sel_hi:[1,0]
	s_nop 0
	v_pk_mul_f32 v[136:137], v[8:9], v[138:139] op_sel_hi:[1,0]
	v_pk_mul_f32 v[134:135], v[6:7], v[138:139] op_sel_hi:[1,0]
	v_pk_mul_f32 v[138:139], v[2:3], v[138:139] op_sel_hi:[1,0]
	v_cvt_pk_bf16_f32 v134, v134, v135
	v_cvt_pk_bf16_f32 v135, v136, v137
	s_nop 0
	v_cvt_pk_bf16_f32 v136, v138, v139
	v_cvt_pk_bf16_f32 v137, v140, v141
	global_store_dwordx4 v[36:37], v[134:137], off offset:256 nt
